# rows1: parameter vectors preloaded (g_post_mix / g_pre_ffn once per phase, gt / sh / sc once per pass with the data loads); the 38 per-chunk reloads of a pass become register copies and their waits ar
# speedup vs baseline: 1.0091x; 1.0091x over previous
; DI float bflo(unsigned u) { return __uint_as_float(u << 16); }
; DI float bfhi(unsigned u) { return __uint_as_float(u & 0xffff0000u); }
; DI void phase_rows1(const Params& p, int bid, int nb) {
;     ...
;   for (int row0 = gw * 2; row0 < T_; row0 += nw * 2) {
;     const int b = row0 >> 13;
;     f32x4 v[2][4], xv[2][4];
; #pragma unroll
;     for (int r = 0; r < 2; ++r)
; #pragma unroll
;       for (int i = 0; i < 4; ++i) { const u32x2 mb = *(const u32x2*)(mixb + (size_t)(row0 + r) * 1024 + 4 * lane + 256 * i);
;         v[r][i] = (f32x4){bflo(mb[0]), bfhi(mb[0]), bflo(mb[1]), bfhi(mb[1])}; xv[r][i] = ((const f32x4*)(p.x + (size_t)(row0 + r) * 1024))[lane + 64 * i]; }
; #pragma unroll
;     for (int r = 0; r < 2; ++r) {
;       f32x4* mr = (f32x4*)(p.out + (size_t)(row0 + r) * 1024);
;       float ss = 0.f;
; #pragma unroll
;       for (int i = 0; i < 4; ++i) ss += v[r][i][0] * v[r][i][0] + v[r][i][1] * v[r][i][1] + v[r][i][2] * v[r][i][2] + v[r][i][3] * v[r][i][3];
;       ss = wave_sum(ss);
;       const float rstd = rsqrtf(ss * (1.f / 1024.f) + 1e-6f);
;       float s2 = 0.f;
; #pragma unroll
;       for (int i = 0; i < 4; ++i) {
;         const int col = 4 * lane + 256 * i;
;         const f32x4 g4 = *(const f32x4*)(p.g_post_mix + col), gt = *(const f32x4*)(mod + b * 6144 + 2048 + col);
.LBB0_1532:
	s_or_b64 exec, exec, s[0:1]
	s_waitcnt lgkmcnt(0)
	v_mov_b32_e32 v0, v206
	v_mov_b32_e32 v1, v206
	s_barrier
	v_lshlrev_b32_e32 v208, 3, v176
	v_ashrrev_i32_e32 v1, 5, v1
	v_and_b32_e32 v1, -2, v1
	v_add_u32_e32 v20, v1, v208
	s_mov_b32 s0, 0x8000
	v_cmp_gt_i32_e32 vcc, s0, v20
	s_and_saveexec_b64 s[0:1], vcc
	s_cbranch_execz .LBB0_1535
	v_and_b32_e32 v2, 64, v158
	v_add_u32_e32 v2, 64, v2
	v_xor_b32_e32 v3, 32, v158
	v_cmp_lt_i32_e32 vcc, v3, v2
	v_ashrrev_i32_e32 v21, 31, v20
	v_and_b32_e32 v1, 63, v0
	v_cndmask_b32_e32 v3, v158, v3, vcc
	v_lshlrev_b32_e32 v35, 2, v3
	v_xor_b32_e32 v3, 16, v158
	v_cmp_lt_i32_e32 vcc, v3, v2
	v_lshlrev_b64 v[8:9], 11, v[20:21]
	v_lshl_or_b32 v8, v1, 3, v8
	v_cndmask_b32_e32 v3, v158, v3, vcc
	v_lshlrev_b32_e32 v84, 2, v3
	v_xor_b32_e32 v3, 8, v158
	v_cmp_lt_i32_e32 vcc, v3, v2
	v_lshlrev_b32_e32 v0, 2, v1
	s_lshl_b32 s4, s86, 4
	v_cndmask_b32_e32 v3, v158, v3, vcc
	v_lshlrev_b32_e32 v85, 2, v3
	v_xor_b32_e32 v3, 4, v158
	v_cmp_lt_i32_e32 vcc, v3, v2
	v_lshl_add_u64 v[8:9], s[84:85], 0, v[8:9]
	s_mov_b64 s[2:3], 0x6000e00
	v_cndmask_b32_e32 v3, v158, v3, vcc
	v_lshlrev_b32_e32 v86, 2, v3
	v_xor_b32_e32 v3, 2, v158
	v_cmp_lt_i32_e32 vcc, v3, v2
	v_mov_b32_e32 v23, 0
	v_or_b32_e32 v4, 0x200, v0
	v_cndmask_b32_e32 v3, v158, v3, vcc
	v_lshlrev_b32_e32 v87, 2, v3
	v_xor_b32_e32 v3, 1, v158
	v_cmp_lt_i32_e32 vcc, v3, v2
	v_or_b32_e32 v6, 0x300, v0
	v_lshlrev_b32_e32 v22, 4, v1
	v_cndmask_b32_e32 v2, v158, v3, vcc
	v_lshlrev_b32_e32 v88, 2, v2
	v_or_b32_e32 v2, 0x100, v0
	v_lshl_add_u64 v[28:29], v[8:9], 0, s[2:3]
	s_ashr_i32 s5, s4, 31
	v_lshlrev_b64 v[8:9], 12, v[20:21]
	v_lshl_add_u64 v[24:25], s[46:47], 0, v[22:23]
	v_lshl_add_u64 v[26:27], s[52:53], 0, v[22:23]
	global_load_dwordx4 v[210:213], v[24:25], off
	global_load_dwordx4 v[214:217], v[24:25], off offset:1024
	global_load_dwordx4 v[218:221], v[24:25], off offset:2048
	global_load_dwordx4 v[222:225], v[24:25], off offset:3072
	global_load_dwordx4 v[226:229], v[26:27], off
	global_load_dwordx4 v[230:233], v[26:27], off offset:1024
	global_load_dwordx4 v[234:237], v[26:27], off offset:2048
	global_load_dwordx4 v[238:241], v[26:27], off offset:3072
	s_lshl_b64 s[6:7], s[4:5], 11
	v_lshl_add_u64 v[30:31], s[66:67], 0, v[8:9]
	s_lshl_b64 s[8:9], s[4:5], 12
	v_lshl_add_u64 v[32:33], s[36:37], 0, v[8:9]
	s_mov_b64 s[10:11], 0
	s_movk_i32 s2, 0x1000
	s_mov_b64 s[12:13], 0x2000
	s_mov_b64 s[14:15], 0x3000
	s_mov_b64 s[16:17], 0x4000
	v_mov_b32_e32 v34, 0x358637bd
	s_mov_b32 s24, 0x3a800000
	s_mov_b32 s3, 0x800000
	v_lshlrev_b32_e32 v36, 2, v0
	v_mov_b32_e32 v37, v23
	v_lshlrev_b32_e32 v38, 2, v2
	v_mov_b32_e32 v39, v23
	v_lshlrev_b32_e32 v40, 2, v4
	v_mov_b32_e32 v41, v23
	v_lshlrev_b32_e32 v42, 2, v6
	v_mov_b32_e32 v43, v23
	s_brev_b32 s5, 63
	s_movk_i32 s18, 0x7fff
.LBB0_1534:
	global_load_dwordx2 v[62:63], v[28:29], off offset:-3072
	global_load_dwordx2 v[60:61], v[28:29], off offset:-3584
	global_load_dwordx2 v[58:59], v[28:29], off offset:-2048
	global_load_dwordx2 v[56:57], v[28:29], off offset:-2560
	v_ashrrev_i32_e32 v2, 13, v20
	v_mul_i32_i24_e32 v64, 0x1800, v2
	v_add_co_u32_e32 v44, vcc, s5, v28
	v_ashrrev_i32_e32 v65, 31, v64
	v_lshl_add_u64 v[0:1], v[32:33], 0, v[22:23]
	v_addc_co_u32_e32 v45, vcc, -1, v29, vcc
	v_lshl_add_u64 v[76:77], v[64:65], 2, s[20:21]
	global_load_dwordx2 v[52:53], v[28:29], off offset:-1536
	global_load_dwordx2 v[54:55], v[28:29], off offset:-1024
	global_load_dwordx2 v[48:49], v[28:29], off offset:-512
	global_load_dwordx2 v[50:51], v[28:29], off
	global_load_dwordx4 v[16:19], v[24:25], off
	global_load_dwordx4 v[66:69], v[0:1], off
	global_load_dwordx4 v[90:93], v[0:1], off offset:1024
	global_load_dwordx4 v[94:97], v[0:1], off offset:2048
	global_load_dwordx4 v[98:101], v[0:1], off offset:3072
	v_add_co_u32_e32 v0, vcc, 0x1000, v0
	v_lshl_add_u64 v[78:79], v[76:77], 0, s[12:13]
	s_nop 0
	v_addc_co_u32_e32 v1, vcc, 0, v1, vcc
	v_lshl_add_u64 v[74:75], v[78:79], 0, v[36:37]
	global_load_dwordx4 v[12:15], v[0:1], off
	global_load_dwordx4 v[8:11], v[0:1], off offset:1024
	global_load_dwordx4 v[4:7], v[0:1], off offset:2048
	s_nop 0
	global_load_dwordx4 v[0:3], v[0:1], off offset:3072
	v_lshl_add_u64 v[46:47], v[30:31], 0, v[22:23]
	global_load_dwordx4 v[70:73], v[74:75], off
	v_lshl_add_u64 v[64:65], v[78:79], 0, v[38:39]
	v_lshl_add_u64 v[110:111], v[76:77], 0, s[14:15]
	v_lshl_add_u64 v[128:129], v[76:77], 0, s[16:17]
	v_add_u32_e32 v20, s4, v20
	v_lshl_add_u64 v[28:29], v[28:29], 0, s[6:7]
	v_lshl_add_u64 v[30:31], v[30:31], 0, s[8:9]
	v_lshl_add_u64 v[32:33], v[32:33], 0, s[8:9]
	v_lshl_add_u64 v[196:197], v[76:77], 0, v[36:37]
	v_lshl_add_u64 v[198:199], v[196:197], 0, s[12:13]
	v_lshl_add_u64 v[200:201], v[196:197], 0, s[14:15]
	v_lshl_add_u64 v[202:203], v[196:197], 0, s[16:17]
	global_load_dwordx4 v[130:133], v[198:199], off
	global_load_dwordx4 v[134:137], v[198:199], off offset:1024
	global_load_dwordx4 v[138:141], v[198:199], off offset:2048
	global_load_dwordx4 v[142:145], v[198:199], off offset:3072
	global_load_dwordx4 v[160:163], v[200:201], off
	global_load_dwordx4 v[164:167], v[200:201], off offset:1024
	global_load_dwordx4 v[168:171], v[200:201], off offset:2048
	global_load_dwordx4 v[172:175], v[200:201], off offset:3072
	global_load_dwordx4 v[178:181], v[202:203], off
	global_load_dwordx4 v[182:185], v[202:203], off offset:1024
	global_load_dwordx4 v[186:189], v[202:203], off offset:2048
	global_load_dwordx4 v[192:195], v[202:203], off offset:3072
	s_waitcnt vmcnt(17)
	v_and_b32_e32 v115, 0xffff0000, v62
	s_waitcnt vmcnt(16)
	v_and_b32_e32 v114, 0xffff0000, v60
	v_lshlrev_b32_e32 v113, 16, v62
	v_lshlrev_b32_e32 v112, 16, v60
	s_waitcnt vmcnt(14)
; DI void phase_rows1(const Params& p, int bid, int nb) {
;     ...
;     for (int r = 0; r < 2; ++r) {
;       f32x4* mr = (f32x4*)(p.out + (size_t)(row0 + r) * 1024);
;       float ss = 0.f;
; #pragma unroll
;       for (int i = 0; i < 4; ++i) ss += v[r][i][0] * v[r][i][0] + v[r][i][1] * v[r][i][1] + v[r][i][2] * v[r][i][2] + v[r][i][3] * v[r][i][3];
;       ss = wave_sum(ss);
;       const float rstd = rsqrtf(ss * (1.f / 1024.f) + 1e-6f);
;       float s2 = 0.f;
; #pragma unroll
;       for (int i = 0; i < 4; ++i) {
;         const int col = 4 * lane + 256 * i;
;         const f32x4 g4 = *(const f32x4*)(p.g_post_mix + col), gt = *(const f32x4*)(mod + b * 6144 + 2048 + col);
;         v[r][i] = xv[r][i] + gt * (v[r][i] * rstd * g4);
;         mr[lane + 64 * i] = v[r][i];
;         s2 += v[r][i][0] * v[r][i][0] + v[r][i][1] * v[r][i][1] + v[r][i][2] * v[r][i][2] + v[r][i][3] * v[r][i][3];
;       }
	v_lshlrev_b32_e32 v120, 16, v56
	v_and_b32_e32 v123, 0xffff0000, v58
	v_and_b32_e32 v122, 0xffff0000, v56
	v_lshlrev_b32_e32 v124, 16, v57
	v_and_b32_e32 v126, 0xffff0000, v57
	v_pk_mul_f32 v[56:57], v[114:115], v[114:115]
	v_lshlrev_b32_e32 v117, 16, v63
	v_lshlrev_b32_e32 v116, 16, v61
	v_lshlrev_b32_e32 v121, 16, v58
	v_lshlrev_b32_e32 v125, 16, v59
	v_and_b32_e32 v127, 0xffff0000, v59
	v_pk_mul_f32 v[58:59], v[122:123], v[122:123]
	v_pk_fma_f32 v[56:57], v[112:113], v[112:113], v[56:57]
	v_and_b32_e32 v119, 0xffff0000, v63
	v_and_b32_e32 v118, 0xffff0000, v61
	v_pk_fma_f32 v[58:59], v[120:121], v[120:121], v[58:59]
	v_pk_fma_f32 v[56:57], v[116:117], v[116:117], v[56:57]
	v_pk_fma_f32 v[58:59], v[124:125], v[124:125], v[58:59]
	v_pk_fma_f32 v[56:57], v[118:119], v[118:119], v[56:57]
	v_pk_fma_f32 v[58:59], v[126:127], v[126:127], v[58:59]
	v_add_f32_e32 v21, v56, v57
	v_add_f32_e32 v21, v21, v58
	v_add_f32_e32 v21, v21, v59
	ds_bpermute_b32 v56, v35, v21
	v_mov_b32_e32 v60, v116
	v_mov_b32_e32 v61, v118
	v_mov_b32_e32 v62, v112
	v_mov_b32_e32 v63, v114
	s_waitcnt lgkmcnt(0)
	v_add_f32_e32 v21, v21, v56
	ds_bpermute_b32 v56, v84, v21
	v_mov_b32_e32 v114, v113
	v_mov_b32_e32 v118, v117
	s_waitcnt vmcnt(12)
	v_lshlrev_b32_e32 v81, 16, v54
	v_lshlrev_b32_e32 v80, 16, v52
	s_waitcnt lgkmcnt(0)
	v_add_f32_e32 v21, v21, v56
	ds_bpermute_b32 v56, v85, v21
	v_and_b32_e32 v77, 0xffff0000, v54
	v_and_b32_e32 v76, 0xffff0000, v52
	v_lshlrev_b32_e32 v83, 16, v55
	v_lshlrev_b32_e32 v82, 16, v53
	s_waitcnt lgkmcnt(0)
	v_add_f32_e32 v21, v21, v56
	ds_bpermute_b32 v56, v86, v21
	s_waitcnt lgkmcnt(0)
	v_add_f32_e32 v21, v21, v56
	ds_bpermute_b32 v56, v87, v21
	s_waitcnt lgkmcnt(0)
	v_add_f32_e32 v21, v21, v56
	ds_bpermute_b32 v56, v88, v21
	s_waitcnt lgkmcnt(0)
	v_add_f32_e32 v21, v21, v56
	v_fmamk_f32 v21, v21, 0x3a800000, v34
	v_mul_f32_e32 v56, 0x4b800000, v21
	v_cmp_gt_f32_e32 vcc, s3, v21
	s_nop 1
	v_cndmask_b32_e32 v21, v21, v56, vcc
	v_rsq_f32_e32 v21, v21
	s_nop 0
	v_mul_f32_e32 v56, 0x45800000, v21
	v_cndmask_b32_e32 v112, v21, v56, vcc
	v_pk_mul_f32 v[56:57], v[112:113], v[60:61] op_sel_hi:[0,1]
	v_pk_mul_f32 v[58:59], v[112:113], v[62:63] op_sel_hi:[0,1]
	s_waitcnt vmcnt(9)
	v_pk_mul_f32 v[16:17], v[16:17], v[58:59]
	v_pk_mul_f32 v[18:19], v[18:19], v[56:57]
	s_waitcnt vmcnt(0)
	v_pk_fma_f32 v[102:103], v[70:71], v[16:17], v[66:67]
	v_pk_fma_f32 v[104:105], v[72:73], v[18:19], v[68:69]
	global_store_dwordx4 v[46:47], v[102:105], off
	v_mov_b32_e32 v66, v214
	v_mov_b32_e32 v67, v215
	v_mov_b32_e32 v68, v216
	v_mov_b32_e32 v69, v217
	v_mov_b32_e32 v106, v134
	v_mov_b32_e32 v107, v135
	v_mov_b32_e32 v108, v136
	v_mov_b32_e32 v109, v137
	v_lshl_add_u64 v[72:73], v[78:79], 0, v[40:41]
	v_lshl_add_u64 v[60:61], v[78:79], 0, v[42:43]
	v_and_b32_e32 v79, 0xffff0000, v55
	v_and_b32_e32 v78, 0xffff0000, v53
	v_pk_mul_f32 v[52:53], v[112:113], v[114:115] op_sel_hi:[0,1]
	v_pk_mul_f32 v[54:55], v[112:113], v[118:119] op_sel_hi:[0,1]
	v_lshlrev_b32_e32 v63, 16, v50
	v_lshlrev_b32_e32 v62, 16, v48
	v_lshlrev_b32_e32 v71, 16, v51
	v_lshlrev_b32_e32 v70, 16, v49
	v_pk_mul_f32 v[114:115], v[76:77], v[76:77]
	v_mov_b32_e32 v118, v102
	v_pk_fma_f32 v[114:115], v[80:81], v[80:81], v[114:115]
	v_lshl_add_u64 v[58:59], v[128:129], 0, v[36:37]
	v_pk_fma_f32 v[114:115], v[82:83], v[82:83], v[114:115]
	v_lshl_add_u64 v[56:57], v[110:111], 0, v[36:37]
	v_pk_fma_f32 v[114:115], v[78:79], v[78:79], v[114:115]
	v_lshl_add_u64 v[16:17], v[110:111], 0, v[38:39]
	v_lshl_add_u64 v[18:19], v[128:129], 0, v[38:39]
	v_pk_mul_f32 v[54:55], v[68:69], v[54:55]
	v_pk_mul_f32 v[52:53], v[66:67], v[52:53]
	v_pk_fma_f32 v[54:55], v[108:109], v[54:55], v[92:93]
	v_pk_fma_f32 v[52:53], v[106:107], v[52:53], v[90:91]
	global_store_dwordx4 v[46:47], v[52:55], off offset:1024
	v_mov_b32_e32 v90, v218
	v_mov_b32_e32 v91, v219
	v_mov_b32_e32 v92, v220
	v_mov_b32_e32 v93, v221
	v_mov_b32_e32 v106, v138
	v_mov_b32_e32 v107, v139
	v_mov_b32_e32 v108, v140
	v_mov_b32_e32 v109, v141
	v_and_b32_e32 v67, 0xffff0000, v50
	v_and_b32_e32 v66, 0xffff0000, v48
	v_and_b32_e32 v69, 0xffff0000, v51
	v_and_b32_e32 v68, 0xffff0000, v49
	v_mov_b32_e32 v48, v120
	v_mov_b32_e32 v49, v122
	v_mov_b32_e32 v50, v124
	v_mov_b32_e32 v51, v126
	v_pk_mul_f32 v[48:49], v[112:113], v[48:49] op_sel_hi:[0,1]
	v_pk_mul_f32 v[50:51], v[112:113], v[50:51] op_sel_hi:[0,1]
	v_mov_b32_e32 v122, v121
	v_mov_b32_e32 v120, v103
	v_mov_b32_e32 v121, v53
	v_mov_b32_e32 v126, v125
	v_mov_b32_e32 v119, v52
	v_pk_mul_f32 v[120:121], v[120:121], v[120:121]
	v_mov_b32_e32 v124, v105
	v_pk_fma_f32 v[118:119], v[118:119], v[118:119], v[120:121]
	v_mov_b32_e32 v125, v55
	v_pk_mul_f32 v[116:117], v[66:67], v[66:67]
	v_pk_mul_f32 v[50:51], v[92:93], v[50:51]
	v_pk_mul_f32 v[48:49], v[90:91], v[48:49]
	v_pk_fma_f32 v[92:93], v[108:109], v[50:51], v[96:97]
	v_pk_fma_f32 v[90:91], v[106:107], v[48:49], v[94:95]
	global_store_dwordx4 v[46:47], v[90:93], off offset:2048
	v_mov_b32_e32 v48, v222
	v_mov_b32_e32 v49, v223
	v_mov_b32_e32 v50, v224
	v_mov_b32_e32 v51, v225
	v_mov_b32_e32 v94, v142
	v_mov_b32_e32 v95, v143
	v_mov_b32_e32 v96, v144
	v_mov_b32_e32 v97, v145
	v_pk_mul_f32 v[108:109], v[112:113], v[122:123] op_sel_hi:[0,1]
	v_pk_mul_f32 v[112:113], v[112:113], v[126:127] op_sel_hi:[0,1]
	v_mov_b32_e32 v122, v104
	v_mov_b32_e32 v123, v54
	v_pk_fma_f32 v[118:119], v[122:123], v[122:123], v[118:119]
	v_mov_b32_e32 v106, v114
	v_pk_fma_f32 v[118:119], v[124:125], v[124:125], v[118:119]
	v_mov_b32_e32 v123, v91
	v_mov_b32_e32 v107, v118
	v_mov_b32_e32 v118, v115
	v_pk_add_f32 v[118:119], v[106:107], v[118:119]
	v_mov_b32_e32 v121, v90
; DI unsigned pk2(float lo, float hi) { f32x2 v = {lo, hi}; bf16x2_t b = __builtin_convertvector(v, bf16x2_t); return __builtin_bit_cast(unsigned, b); }
; DI void phase_rows1(const Params& p, int bid, int nb) {
;     ...
;         mr[lane + 64 * i] = v[r][i];
;         s2 += v[r][i][0] * v[r][i][0] + v[r][i][1] * v[r][i][1] + v[r][i][2] * v[r][i][2] + v[r][i][3] * v[r][i][3];
;       }
;       s2 = wave_sum(s2);
;       const float rstd2 = rsqrtf(s2 * (1.f / 1024.f) + 1e-6f);
; #pragma unroll
;       for (int i = 0; i < 4; ++i) {
;         const int col = 4 * lane + 256 * i;
;         const f32x4 g4 = *(const f32x4*)(p.g_pre_ffn + col), sh = *(const f32x4*)(mod + b * 6144 + 3072 + col), sc = *(const f32x4*)(mod + b * 6144 + 4096 + col);
;         const f32x4 y = (v[r][i] * rstd2 * g4) * (1.f + sc) + sh;
;         u32x2 o = {pk2(y[0], y[1]), pk2(y[2], y[3])};
;         *(u32x2*)(h2 + (size_t)(row0 + r) * 1024 + col) = o;
	v_pk_fma_f32 v[116:117], v[62:63], v[62:63], v[116:117]
	v_mov_b32_e32 v125, v92
	v_pk_fma_f32 v[116:117], v[70:71], v[70:71], v[116:117]
	v_mov_b32_e32 v127, v93
	v_pk_fma_f32 v[116:117], v[68:69], v[68:69], v[116:117]
	v_pk_mul_f32 v[50:51], v[50:51], v[112:113]
	v_pk_mul_f32 v[48:49], v[48:49], v[108:109]
	v_pk_fma_f32 v[96:97], v[96:97], v[50:51], v[100:101]
	v_pk_fma_f32 v[94:95], v[94:95], v[48:49], v[98:99]
	global_store_dwordx4 v[46:47], v[94:97], off offset:3072
	v_mov_b32_e32 v48, v178
	v_mov_b32_e32 v49, v179
	v_mov_b32_e32 v50, v180
	v_mov_b32_e32 v51, v181
	v_mov_b32_e32 v98, v226
	v_mov_b32_e32 v99, v227
	v_mov_b32_e32 v100, v228
	v_mov_b32_e32 v101, v229
	v_mov_b32_e32 v106, v160
	v_mov_b32_e32 v107, v161
	v_mov_b32_e32 v108, v162
	v_mov_b32_e32 v109, v163
	v_mov_b32_e32 v122, v95
	v_mov_b32_e32 v120, v94
	v_pk_mul_f32 v[112:113], v[122:123], v[122:123]
	v_mov_b32_e32 v124, v96
	v_pk_fma_f32 v[112:113], v[120:121], v[120:121], v[112:113]
	v_mov_b32_e32 v126, v97
	v_pk_fma_f32 v[112:113], v[124:125], v[124:125], v[112:113]
	v_mov_b32_e32 v114, v116
	v_pk_fma_f32 v[112:113], v[126:127], v[126:127], v[112:113]
	v_pk_add_f32 v[50:51], v[50:51], 1.0 op_sel_hi:[1,0]
	v_mov_b32_e32 v115, v113
	v_pk_mov_b32 v[112:113], v[116:117], v[112:113] op_sel:[1,0]
	v_pk_add_f32 v[114:115], v[118:119], v[114:115]
	v_pk_add_f32 v[48:49], v[48:49], 1.0 op_sel_hi:[1,0]
	v_pk_add_f32 v[112:113], v[114:115], v[112:113]
	ds_bpermute_b32 v115, v35, v113
	ds_bpermute_b32 v114, v35, v112
	s_waitcnt lgkmcnt(0)
	v_pk_add_f32 v[112:113], v[112:113], v[114:115]
	ds_bpermute_b32 v115, v84, v113
	ds_bpermute_b32 v114, v84, v112
	s_waitcnt lgkmcnt(0)
	v_pk_add_f32 v[112:113], v[112:113], v[114:115]
	ds_bpermute_b32 v115, v85, v113
	ds_bpermute_b32 v114, v85, v112
	s_waitcnt lgkmcnt(0)
	v_pk_add_f32 v[112:113], v[112:113], v[114:115]
	ds_bpermute_b32 v115, v86, v113
	ds_bpermute_b32 v114, v86, v112
	s_waitcnt lgkmcnt(0)
	v_pk_add_f32 v[112:113], v[112:113], v[114:115]
	ds_bpermute_b32 v115, v87, v113
	ds_bpermute_b32 v114, v87, v112
	s_waitcnt lgkmcnt(0)
	v_pk_add_f32 v[112:113], v[112:113], v[114:115]
	ds_bpermute_b32 v115, v88, v113
	ds_bpermute_b32 v114, v88, v112
	s_waitcnt lgkmcnt(0)
	v_pk_add_f32 v[112:113], v[112:113], v[114:115]
	s_nop 0
	v_pk_fma_f32 v[112:113], v[112:113], s[24:25], v[34:35] op_sel_hi:[1,0,0]
	s_nop 0
	v_mul_f32_e32 v21, 0x4b800000, v113
	v_cmp_gt_f32_e32 vcc, s3, v113
	s_nop 1
	v_cndmask_b32_e32 v21, v113, v21, vcc
	v_rsq_f32_e32 v21, v21
	s_nop 0
	v_mul_f32_e32 v89, 0x45800000, v21
	v_cndmask_b32_e32 v114, v21, v89, vcc
	v_pk_mul_f32 v[104:105], v[104:105], v[114:115] op_sel_hi:[1,0]
	v_pk_mul_f32 v[102:103], v[102:103], v[114:115] op_sel_hi:[1,0]
	v_pk_mul_f32 v[100:101], v[100:101], v[104:105]
	v_pk_mul_f32 v[98:99], v[98:99], v[102:103]
	v_pk_fma_f32 v[50:51], v[50:51], v[100:101], v[108:109]
	v_pk_fma_f32 v[48:49], v[48:49], v[98:99], v[106:107]
	v_pk_mul_f32 v[54:55], v[54:55], v[114:115] op_sel_hi:[1,0]
	v_cvt_pk_bf16_f32 v48, v48, v49
	v_cvt_pk_bf16_f32 v49, v50, v51
	global_store_dwordx2 v[44:45], v[48:49], off offset:-3584
	v_mov_b32_e32 v98, v230
	v_mov_b32_e32 v99, v231
	v_mov_b32_e32 v100, v232
	v_mov_b32_e32 v101, v233
	v_mov_b32_e32 v102, v182
	v_mov_b32_e32 v103, v183
	v_mov_b32_e32 v104, v184
	v_mov_b32_e32 v105, v185
	v_mov_b32_e32 v106, v164
	v_mov_b32_e32 v107, v165
	v_mov_b32_e32 v108, v166
	v_mov_b32_e32 v109, v167
	v_pk_mul_f32 v[52:53], v[52:53], v[114:115] op_sel_hi:[1,0]
	v_lshl_add_u64 v[48:49], v[110:111], 0, v[40:41]
	v_lshl_add_u64 v[50:51], v[128:129], 0, v[40:41]
	v_pk_mul_f32 v[92:93], v[92:93], v[114:115] op_sel_hi:[1,0]
	v_pk_mul_f32 v[90:91], v[90:91], v[114:115] op_sel_hi:[1,0]
	v_pk_mul_f32 v[96:97], v[96:97], v[114:115] op_sel_hi:[1,0]
	v_pk_mul_f32 v[94:95], v[94:95], v[114:115] op_sel_hi:[1,0]
	v_add_co_u32_e32 v46, vcc, s2, v46
	v_mul_f32_e32 v21, 0x4b800000, v112
	s_nop 0
	v_addc_co_u32_e32 v47, vcc, 0, v47, vcc
	v_cmp_gt_f32_e32 vcc, s3, v112
	v_pk_mul_f32 v[52:53], v[98:99], v[52:53]
	v_pk_mul_f32 v[54:55], v[100:101], v[54:55]
	v_pk_add_f32 v[98:99], v[104:105], 1.0 op_sel_hi:[1,0]
	v_pk_add_f32 v[100:101], v[102:103], 1.0 op_sel_hi:[1,0]
	v_pk_fma_f32 v[54:55], v[98:99], v[54:55], v[108:109]
	v_pk_fma_f32 v[52:53], v[100:101], v[52:53], v[106:107]
	v_cndmask_b32_e32 v21, v112, v21, vcc
	v_cvt_pk_bf16_f32 v52, v52, v53
	v_cvt_pk_bf16_f32 v53, v54, v55
	global_store_dwordx2 v[44:45], v[52:53], off offset:-3072
	v_mov_b32_e32 v98, v234
	v_mov_b32_e32 v99, v235
	v_mov_b32_e32 v100, v236
	v_mov_b32_e32 v101, v237
	v_mov_b32_e32 v102, v186
	v_mov_b32_e32 v103, v187
	v_mov_b32_e32 v104, v188
	v_mov_b32_e32 v105, v189
	v_mov_b32_e32 v106, v168
	v_mov_b32_e32 v107, v169
	v_mov_b32_e32 v108, v170
	v_mov_b32_e32 v109, v171
	v_lshl_add_u64 v[52:53], v[110:111], 0, v[42:43]
	v_lshl_add_u64 v[54:55], v[128:129], 0, v[42:43]
	v_rsq_f32_e32 v21, v21
	v_pk_mul_f32 v[90:91], v[98:99], v[90:91]
	v_pk_mul_f32 v[92:93], v[100:101], v[92:93]
	v_pk_add_f32 v[98:99], v[104:105], 1.0 op_sel_hi:[1,0]
	v_pk_add_f32 v[100:101], v[102:103], 1.0 op_sel_hi:[1,0]
	v_pk_fma_f32 v[92:93], v[98:99], v[92:93], v[108:109]
	v_pk_fma_f32 v[90:91], v[100:101], v[90:91], v[106:107]
	s_nop 0
	v_cvt_pk_bf16_f32 v90, v90, v91
	v_cvt_pk_bf16_f32 v91, v92, v93
	global_store_dwordx2 v[44:45], v[90:91], off offset:-2560
	v_mov_b32_e32 v90, v238
	v_mov_b32_e32 v91, v239
	v_mov_b32_e32 v92, v240
	v_mov_b32_e32 v93, v241
	s_nop 0
	v_mov_b32_e32 v98, v192
	v_mov_b32_e32 v99, v193
	v_mov_b32_e32 v100, v194
	v_mov_b32_e32 v101, v195
	v_mov_b32_e32 v102, v172
	v_mov_b32_e32 v103, v173
	v_mov_b32_e32 v104, v174
	v_mov_b32_e32 v105, v175
; DI void phase_rows1(const Params& p, int bid, int nb) {
;     ...
;       for (int i = 0; i < 4; ++i) {
;         const int col = 4 * lane + 256 * i;
;         const f32x4 g4 = *(const f32x4*)(p.g_post_mix + col), gt = *(const f32x4*)(mod + b * 6144 + 2048 + col);
;         v[r][i] = xv[r][i] + gt * (v[r][i] * rstd * g4);
;         mr[lane + 64 * i] = v[r][i];
;         s2 += v[r][i][0] * v[r][i][0] + v[r][i][1] * v[r][i][1] + v[r][i][2] * v[r][i][2] + v[r][i][3] * v[r][i][3];
;       }
;       s2 = wave_sum(s2);
;       const float rstd2 = rsqrtf(s2 * (1.f / 1024.f) + 1e-6f);
; #pragma unroll
;       for (int i = 0; i < 4; ++i) {
;         const int col = 4 * lane + 256 * i;
;         const f32x4 g4 = *(const f32x4*)(p.g_pre_ffn + col), sh = *(const f32x4*)(mod + b * 6144 + 3072 + col), sc = *(const f32x4*)(mod + b * 6144 + 4096 + col);
	v_pk_mul_f32 v[90:91], v[90:91], v[94:95]
	v_pk_mul_f32 v[92:93], v[92:93], v[96:97]
	v_pk_add_f32 v[94:95], v[100:101], 1.0 op_sel_hi:[1,0]
	v_pk_add_f32 v[96:97], v[98:99], 1.0 op_sel_hi:[1,0]
	v_pk_fma_f32 v[92:93], v[94:95], v[92:93], v[104:105]
	v_pk_fma_f32 v[90:91], v[96:97], v[90:91], v[102:103]
	v_mov_b32_e32 v98, v82
	v_cvt_pk_bf16_f32 v90, v90, v91
	v_cvt_pk_bf16_f32 v91, v92, v93
	global_store_dwordx2 v[44:45], v[90:91], off offset:-2048
	v_mov_b32_e32 v90, v210
	v_mov_b32_e32 v91, v211
	v_mov_b32_e32 v92, v212
	v_mov_b32_e32 v93, v213
	s_nop 0
	v_mov_b32_e32 v94, v130
	v_mov_b32_e32 v95, v131
	v_mov_b32_e32 v96, v132
	v_mov_b32_e32 v97, v133
	v_mov_b32_e32 v75, v76
	v_mul_f32_e32 v76, 0x45800000, v21
	v_mov_b32_e32 v74, v80
	v_mov_b32_e32 v99, v78
	v_cndmask_b32_e32 v82, v21, v76, vcc
	v_pk_mul_f32 v[74:75], v[82:83], v[74:75] op_sel_hi:[0,1]
	v_pk_mul_f32 v[98:99], v[82:83], v[98:99] op_sel_hi:[0,1]
	v_mov_b32_e32 v76, v81
	v_mov_b32_e32 v78, v83
	v_pk_mul_f32 v[92:93], v[92:93], v[98:99]
	v_pk_mul_f32 v[74:75], v[90:91], v[74:75]
	v_pk_fma_f32 v[14:15], v[96:97], v[92:93], v[14:15]
	v_pk_fma_f32 v[12:13], v[94:95], v[74:75], v[12:13]
	global_store_dwordx4 v[46:47], v[12:15], off
	v_mov_b32_e32 v90, v214
	v_mov_b32_e32 v91, v215
	v_mov_b32_e32 v92, v216
	v_mov_b32_e32 v93, v217
	v_mov_b32_e32 v94, v134
	v_mov_b32_e32 v95, v135
	v_mov_b32_e32 v96, v136
	v_mov_b32_e32 v97, v137
	v_pk_mul_f32 v[64:65], v[82:83], v[76:77] op_sel_hi:[0,1]
	v_pk_mul_f32 v[74:75], v[82:83], v[78:79] op_sel_hi:[0,1]
	v_pk_mul_f32 v[74:75], v[92:93], v[74:75]
	v_pk_mul_f32 v[64:65], v[90:91], v[64:65]
	v_pk_fma_f32 v[10:11], v[96:97], v[74:75], v[10:11]
	v_pk_fma_f32 v[8:9], v[94:95], v[64:65], v[8:9]
	global_store_dwordx4 v[46:47], v[8:11], off offset:1024
	v_mov_b32_e32 v74, v218
	v_mov_b32_e32 v75, v219
	v_mov_b32_e32 v76, v220
	v_mov_b32_e32 v77, v221
	v_mov_b32_e32 v78, v138
	v_mov_b32_e32 v79, v139
	v_mov_b32_e32 v80, v140
	v_mov_b32_e32 v81, v141
	v_mov_b32_e32 v64, v62
	v_mov_b32_e32 v65, v66
	v_mov_b32_e32 v72, v70
	v_mov_b32_e32 v73, v68
	v_pk_mul_f32 v[64:65], v[82:83], v[64:65] op_sel_hi:[0,1]
	v_pk_mul_f32 v[72:73], v[82:83], v[72:73] op_sel_hi:[0,1]
	v_mov_b32_e32 v66, v63
	v_mov_b32_e32 v68, v71
	v_pk_mul_f32 v[62:63], v[82:83], v[68:69] op_sel_hi:[0,1]
	v_mov_b32_e32 v68, v14
	v_mov_b32_e32 v69, v10
	v_mov_b32_e32 v70, v15
	v_mov_b32_e32 v71, v11
	v_pk_mul_f32 v[72:73], v[76:77], v[72:73]
	v_pk_mul_f32 v[64:65], v[74:75], v[64:65]
	v_pk_fma_f32 v[6:7], v[80:81], v[72:73], v[6:7]
	v_pk_fma_f32 v[4:5], v[78:79], v[64:65], v[4:5]
	global_store_dwordx4 v[46:47], v[4:7], off offset:2048
	v_mov_b32_e32 v72, v222
	v_mov_b32_e32 v73, v223
	v_mov_b32_e32 v74, v224
	v_mov_b32_e32 v75, v225
	v_mov_b32_e32 v76, v142
	v_mov_b32_e32 v77, v143
	v_mov_b32_e32 v78, v144
	v_mov_b32_e32 v79, v145
	v_pk_mul_f32 v[60:61], v[82:83], v[66:67] op_sel_hi:[0,1]
	v_mov_b32_e32 v66, v13
	v_mov_b32_e32 v67, v9
	v_mov_b32_e32 v64, v12
	v_mov_b32_e32 v65, v8
	v_pk_mul_f32 v[66:67], v[66:67], v[66:67]
	v_mov_b32_e32 v81, v6
	v_pk_fma_f32 v[64:65], v[64:65], v[64:65], v[66:67]
	v_pk_mul_f32 v[62:63], v[74:75], v[62:63]
	v_pk_mul_f32 v[60:61], v[72:73], v[60:61]
	v_pk_fma_f32 v[64:65], v[68:69], v[68:69], v[64:65]
	v_pk_fma_f32 v[0:1], v[76:77], v[60:61], v[0:1]
	v_pk_fma_f32 v[2:3], v[78:79], v[62:63], v[2:3]
	v_pk_fma_f32 v[64:65], v[70:71], v[70:71], v[64:65]
	global_store_dwordx4 v[46:47], v[0:3], off offset:3072
	v_add_f32_e32 v21, v64, v65
	v_mov_b32_e32 v60, v226
	v_mov_b32_e32 v61, v227
	v_mov_b32_e32 v62, v228
	v_mov_b32_e32 v63, v229
	v_mov_b32_e32 v64, v178
	v_mov_b32_e32 v65, v179
	v_mov_b32_e32 v66, v180
	v_mov_b32_e32 v67, v181
	s_nop 0
	v_mov_b32_e32 v56, v160
	v_mov_b32_e32 v57, v161
	v_mov_b32_e32 v58, v162
	v_mov_b32_e32 v59, v163
	v_mov_b32_e32 v71, v5
	v_mov_b32_e32 v70, v1
	v_mov_b32_e32 v69, v4
	v_mov_b32_e32 v68, v0
	v_pk_mul_f32 v[70:71], v[70:71], v[70:71]
	v_mov_b32_e32 v80, v2
	v_pk_fma_f32 v[68:69], v[68:69], v[68:69], v[70:71]
	v_mov_b32_e32 v47, v7
	v_mov_b32_e32 v46, v3
	v_pk_fma_f32 v[68:69], v[80:81], v[80:81], v[68:69]
	s_nop 0
	v_pk_fma_f32 v[46:47], v[46:47], v[46:47], v[68:69]
	s_nop 0
	v_add_f32_e32 v21, v47, v21
	v_add_f32_e32 v21, v46, v21
	ds_bpermute_b32 v46, v35, v21
	s_waitcnt lgkmcnt(0)
; DI unsigned pk2(float lo, float hi) { f32x2 v = {lo, hi}; bf16x2_t b = __builtin_convertvector(v, bf16x2_t); return __builtin_bit_cast(unsigned, b); }
; DI void phase_rows1(const Params& p, int bid, int nb) {
;     ...
;       s2 = wave_sum(s2);
;       const float rstd2 = rsqrtf(s2 * (1.f / 1024.f) + 1e-6f);
; #pragma unroll
;       for (int i = 0; i < 4; ++i) {
;         const int col = 4 * lane + 256 * i;
;         const f32x4 g4 = *(const f32x4*)(p.g_pre_ffn + col), sh = *(const f32x4*)(mod + b * 6144 + 3072 + col), sc = *(const f32x4*)(mod + b * 6144 + 4096 + col);
;         const f32x4 y = (v[r][i] * rstd2 * g4) * (1.f + sc) + sh;
;         u32x2 o = {pk2(y[0], y[1]), pk2(y[2], y[3])};
;         *(u32x2*)(h2 + (size_t)(row0 + r) * 1024 + col) = o;
;       }
;     }
;   }
	v_add_f32_e32 v21, v21, v46
	ds_bpermute_b32 v46, v84, v21
	s_waitcnt lgkmcnt(0)
	v_add_f32_e32 v21, v21, v46
	ds_bpermute_b32 v46, v85, v21
	s_waitcnt lgkmcnt(0)
	v_add_f32_e32 v21, v21, v46
	ds_bpermute_b32 v46, v86, v21
	s_waitcnt lgkmcnt(0)
	v_add_f32_e32 v21, v21, v46
	ds_bpermute_b32 v46, v87, v21
	s_waitcnt lgkmcnt(0)
	v_add_f32_e32 v21, v21, v46
	ds_bpermute_b32 v46, v88, v21
	s_waitcnt lgkmcnt(0)
	v_add_f32_e32 v21, v21, v46
	v_fmamk_f32 v21, v21, 0x3a800000, v34
	v_mul_f32_e32 v46, 0x4b800000, v21
	v_cmp_gt_f32_e32 vcc, s3, v21
	s_nop 1
	v_cndmask_b32_e32 v21, v21, v46, vcc
	v_rsq_f32_e32 v21, v21
	s_nop 0
	v_mul_f32_e32 v46, 0x45800000, v21
	v_cndmask_b32_e32 v46, v21, v46, vcc
	v_pk_mul_f32 v[14:15], v[14:15], v[46:47] op_sel_hi:[1,0]
	v_pk_mul_f32 v[12:13], v[12:13], v[46:47] op_sel_hi:[1,0]
	v_pk_mul_f32 v[10:11], v[10:11], v[46:47] op_sel_hi:[1,0]
	v_pk_mul_f32 v[8:9], v[8:9], v[46:47] op_sel_hi:[1,0]
	v_pk_mul_f32 v[6:7], v[6:7], v[46:47] op_sel_hi:[1,0]
	v_pk_mul_f32 v[4:5], v[4:5], v[46:47] op_sel_hi:[1,0]
	v_pk_mul_f32 v[2:3], v[2:3], v[46:47] op_sel_hi:[1,0]
	v_pk_mul_f32 v[0:1], v[0:1], v[46:47] op_sel_hi:[1,0]
	v_cmp_lt_i32_e32 vcc, s18, v20
	s_or_b64 s[10:11], vcc, s[10:11]
	v_pk_mul_f32 v[12:13], v[60:61], v[12:13]
	v_pk_mul_f32 v[14:15], v[62:63], v[14:15]
	v_pk_add_f32 v[60:61], v[66:67], 1.0 op_sel_hi:[1,0]
	v_pk_add_f32 v[62:63], v[64:65], 1.0 op_sel_hi:[1,0]
	v_pk_fma_f32 v[14:15], v[60:61], v[14:15], v[58:59]
	v_pk_fma_f32 v[12:13], v[62:63], v[12:13], v[56:57]
	s_nop 0
	v_cvt_pk_bf16_f32 v12, v12, v13
	v_cvt_pk_bf16_f32 v13, v14, v15
	global_store_dwordx2 v[44:45], v[12:13], off offset:-1536
	v_mov_b32_e32 v12, v230
	v_mov_b32_e32 v13, v231
	v_mov_b32_e32 v14, v232
	v_mov_b32_e32 v15, v233
	s_nop 0
	v_mov_b32_e32 v56, v182
	v_mov_b32_e32 v57, v183
	v_mov_b32_e32 v58, v184
	v_mov_b32_e32 v59, v185
	s_nop 0
	v_mov_b32_e32 v16, v164
	v_mov_b32_e32 v17, v165
	v_mov_b32_e32 v18, v166
	v_mov_b32_e32 v19, v167
	v_pk_mul_f32 v[8:9], v[12:13], v[8:9]
	v_pk_mul_f32 v[10:11], v[14:15], v[10:11]
	v_pk_add_f32 v[12:13], v[58:59], 1.0 op_sel_hi:[1,0]
	v_pk_add_f32 v[14:15], v[56:57], 1.0 op_sel_hi:[1,0]
	v_pk_fma_f32 v[10:11], v[12:13], v[10:11], v[18:19]
	v_pk_fma_f32 v[8:9], v[14:15], v[8:9], v[16:17]
	s_nop 0
	v_cvt_pk_bf16_f32 v8, v8, v9
	v_cvt_pk_bf16_f32 v9, v10, v11
	global_store_dwordx2 v[44:45], v[8:9], off offset:-1024
	v_mov_b32_e32 v8, v234
	v_mov_b32_e32 v9, v235
	v_mov_b32_e32 v10, v236
	v_mov_b32_e32 v11, v237
	s_nop 0
	v_mov_b32_e32 v12, v186
	v_mov_b32_e32 v13, v187
	v_mov_b32_e32 v14, v188
	v_mov_b32_e32 v15, v189
	v_mov_b32_e32 v16, v168
	v_mov_b32_e32 v17, v169
	v_mov_b32_e32 v18, v170
	v_mov_b32_e32 v19, v171
	v_pk_mul_f32 v[4:5], v[8:9], v[4:5]
	v_pk_mul_f32 v[6:7], v[10:11], v[6:7]
	v_pk_add_f32 v[8:9], v[14:15], 1.0 op_sel_hi:[1,0]
	v_pk_add_f32 v[10:11], v[12:13], 1.0 op_sel_hi:[1,0]
	v_pk_fma_f32 v[6:7], v[8:9], v[6:7], v[18:19]
	v_pk_fma_f32 v[4:5], v[10:11], v[4:5], v[16:17]
	s_nop 0
	v_cvt_pk_bf16_f32 v4, v4, v5
	v_cvt_pk_bf16_f32 v5, v6, v7
	global_store_dwordx2 v[44:45], v[4:5], off offset:-512
	v_mov_b32_e32 v4, v238
	v_mov_b32_e32 v5, v239
	v_mov_b32_e32 v6, v240
	v_mov_b32_e32 v7, v241
	s_nop 0
	v_mov_b32_e32 v8, v192
	v_mov_b32_e32 v9, v193
	v_mov_b32_e32 v10, v194
	v_mov_b32_e32 v11, v195
	v_mov_b32_e32 v12, v172
	v_mov_b32_e32 v13, v173
	v_mov_b32_e32 v14, v174
	v_mov_b32_e32 v15, v175
	v_pk_mul_f32 v[0:1], v[4:5], v[0:1]
	v_pk_mul_f32 v[2:3], v[6:7], v[2:3]
	v_pk_add_f32 v[4:5], v[10:11], 1.0 op_sel_hi:[1,0]
	v_pk_add_f32 v[6:7], v[8:9], 1.0 op_sel_hi:[1,0]
	v_pk_fma_f32 v[2:3], v[4:5], v[2:3], v[14:15]
	v_pk_fma_f32 v[0:1], v[6:7], v[0:1], v[12:13]
	s_nop 0
	v_cvt_pk_bf16_f32 v0, v0, v1
	v_cvt_pk_bf16_f32 v1, v2, v3
	global_store_dwordx2 v[44:45], v[0:1], off
	s_andn2_b64 exec, exec, s[10:11]
	s_cbranch_execnz .LBB0_1534
